# speedup vs baseline: 1.0812x; 1.0310x over previous
.Lpx_entry:
	v_and_b32_e32 v50, 63, v0
	s_load_dwordx2 s[4:5], s[0:1], 0x50
	v_lshlrev_b32_e32 v1, 4, v0
	v_or_b32_e32 v18, 0x80, v0
	v_lshlrev_b32_e32 v10, 4, v18
	v_or_b32_e32 v20, 0x180, v0
	s_waitcnt lgkmcnt(0)
	global_load_dwordx4 v[2:5], v1, s[4:5]
	global_load_dwordx4 v[6:9], v10, s[4:5]
	v_or_b32_e32 v1, 0x100, v0
	v_lshlrev_b32_e32 v19, 4, v1
	v_lshlrev_b32_e32 v21, 4, v20
	global_load_dwordx4 v[10:13], v19, s[4:5]
	global_load_dwordx4 v[14:17], v21, s[4:5]
	v_lshrrev_b32_e32 v19, 4, v0
	s_sub_i32 s8, s2, 912
	s_lshl_b32 s8, s8, 1
	v_lshrrev_b32_e32 v23, 6, v0
	s_movk_i32 s4, 0x70
	s_movk_i32 s5, 0xf0
	v_mov_b32_e32 v21, 0x80
	s_movk_i32 s6, 0x170
	s_movk_i32 s7, 0x1f0
	v_mov_b32_e32 v22, 0x180
	v_bitop3_b32 v19, v19, 15, v0 bitop3:0x48
	v_lshrrev_b32_e32 v18, 4, v18
	v_lshrrev_b32_e32 v20, 4, v20
	v_or_b32_e32 v23, s8, v23
	s_mov_b32 s3, 0xc350
	v_bitop3_b32 v21, v0, s5, v21 bitop3:0xc8
	v_bitop3_b32 v22, v0, s7, v22 bitop3:0xc8
	v_and_or_b32 v24, v0, s4, v19
	v_xor_b32_e32 v18, v18, v0
	v_and_or_b32 v19, v1, s6, v19
	v_xor_b32_e32 v20, v20, v0
	v_lshlrev_b32_e32 v1, 4, v23
	v_lshlrev_b32_e32 v23, 4, v24
	v_and_or_b32 v18, v18, 15, v21
	v_and_or_b32 v20, v20, 15, v22
	v_cmp_gt_i32_e32 vcc, s3, v1
	v_lshlrev_b32_e32 v19, 4, v19
	v_lshlrev_b32_e32 v18, 4, v18
	v_lshlrev_b32_e32 v20, 4, v20
	s_waitcnt vmcnt(3)
	ds_write_b128 v23, v[2:5]
	s_waitcnt vmcnt(2)
	ds_write_b128 v18, v[6:9]
	s_waitcnt vmcnt(1)
	ds_write_b128 v19, v[10:13]
	s_waitcnt vmcnt(0)
	ds_write_b128 v20, v[14:17]
	s_waitcnt lgkmcnt(0)
	s_barrier
	s_and_saveexec_b64 s[6:7], vcc
	s_cbranch_execz .LBB1_12
	v_and_b32_e32 v51, 15, v0
	s_load_dwordx2 s[4:5], s[0:1], 0x48
	v_or_b32_e32 v46, v1, v51
	v_mov_b32_e32 v2, 0xc34f
	v_cmp_gt_i32_e32 vcc, s3, v46
	v_lshrrev_b32_e32 v1, 4, v50
	v_lshlrev_b32_e32 v42, 5, v1
	v_cndmask_b32_e32 v2, v2, v46, vcc
	v_ashrrev_i32_e32 v3, 31, v2
	v_lshlrev_b64 v[2:3], 9, v[2:3]
	s_waitcnt lgkmcnt(0)
	v_lshl_add_u64 v[2:3], s[4:5], 0, v[2:3]
	v_mov_b32_e32 v43, 0
	v_lshl_add_u64 v[30:31], v[2:3], 0, v[42:43]
	global_load_dwordx4 v[26:29], v[30:31], off offset:16 nt
	global_load_dwordx4 v[34:37], v[30:31], off nt
	global_load_dwordx4 v[18:21], v[30:31], off offset:144 nt
	global_load_dwordx4 v[22:25], v[30:31], off offset:128 nt
	global_load_dwordx4 v[10:13], v[30:31], off offset:272 nt
	global_load_dwordx4 v[14:17], v[30:31], off offset:256 nt
	global_load_dwordx4 v[2:5], v[30:31], off offset:400 nt
	global_load_dwordx4 v[6:9], v[30:31], off offset:384 nt
	s_load_dwordx2 s[4:5], s[0:1], 0x58
	v_bitop3_b32 v30, v1, v0, 15 bitop3:0x78
	v_lshlrev_b32_e32 v31, 8, v51
	v_lshl_or_b32 v38, v30, 4, v31
	ds_read_b128 v[30:33], v38
	ds_read_b128 v[38:41], v38 offset:4096
	v_ashrrev_i32_e32 v47, 31, v46
	v_lshlrev_b64 v[44:45], 8, v[46:47]
	s_waitcnt lgkmcnt(0)
	v_lshl_add_u64 v[44:45], s[4:5], 0, v[44:45]
	v_and_b32_e32 v42, 48, v50
	v_lshlrev_b32_e32 v52, 7, v51
	v_lshl_add_u64 v[48:49], v[44:45], 0, v[42:43]
	s_waitcnt vmcnt(7)
	v_cvt_pk_f16_f32 v44, v26, v27
	s_waitcnt vmcnt(6)
	v_cvt_f16_f32_e32 v54, v34
	v_cvt_f16_f32_e32 v53, v35
	v_cvt_pk_f16_f32 v42, v34, v35
	v_cvt_pk_f16_f32 v43, v36, v37
	v_cvt_pk_f16_f32 v45, v28, v29
	s_and_saveexec_b64 s[4:5], vcc
	s_cbranch_execz .LBB1_4
	global_store_dwordx4 v[48:49], v[42:45], off sc1
.LBB1_4:
	s_or_b64 exec, exec, s[4:5]
	v_cvt_f32_f16_e32 v56, v54
	v_cvt_f32_f16_e32 v53, v53
	v_cvt_f32_f16_sdwa v55, v43 dst_sel:DWORD dst_unused:UNUSED_PAD src0_sel:WORD_1
	v_cvt_f32_f16_e32 v54, v43
	v_sub_f32_e32 v34, v34, v56
	v_sub_f32_e32 v35, v35, v53
	v_mfma_f32_16x16x32_f16 a[0:3], v[30:33], v[42:45], 0
	v_add_f32_e64 v36, v36, -v54
	v_add_f32_e64 v37, v37, -v55
	v_cvt_pk_f16_f32 v34, v34, v35
	v_cvt_pk_f16_f32 v35, v36, v37
	v_cvt_f32_f16_sdwa v37, v44 dst_sel:DWORD dst_unused:UNUSED_PAD src0_sel:WORD_1
	v_cvt_f32_f16_e32 v36, v44
	v_cvt_f32_f16_sdwa v55, v45 dst_sel:DWORD dst_unused:UNUSED_PAD src0_sel:WORD_1
	v_cvt_f32_f16_e32 v54, v45
	v_mfma_f32_16x16x32_f16 a[0:3], v[38:41], v[42:45], a[0:3]
	v_add_f32_e64 v26, v26, -v36
	v_add_f32_e64 v27, v27, -v37
	v_lshlrev_b32_e32 v38, 1, v52
	v_cvt_pk_f16_f32 v36, v26, v27
	v_pk_add_f32 v[26:27], v[28:29], v[54:55] neg_lo:[0,1] neg_hi:[0,1]
	s_waitcnt vmcnt(4)
	v_cvt_f16_f32_e32 v40, v22
	v_cvt_pk_f16_f32 v37, v26, v27
	v_bitop3_b32 v26, v1, v51, 4 bitop3:0x36
	v_cvt_f16_f32_e32 v39, v23
	v_mfma_f32_16x16x32_f16 a[0:3], v[30:33], v[34:37], a[0:3]
	v_lshl_or_b32 v30, v26, 4, v38
	ds_read_b128 v[26:29], v30
	ds_read_b128 v[30:33], v30 offset:4096
	v_cvt_pk_f16_f32 v34, v22, v23
	v_cvt_pk_f16_f32 v35, v24, v25
	v_cvt_pk_f16_f32 v36, v18, v19
	v_cvt_pk_f16_f32 v37, v20, v21
	s_and_saveexec_b64 s[4:5], vcc
	s_cbranch_execz .LBB1_6
	global_store_dwordx4 v[48:49], v[34:37], off offset:64 sc1
.LBB1_6:
	s_or_b64 exec, exec, s[4:5]
	v_cvt_f32_f16_e32 v42, v40
	v_cvt_f32_f16_e32 v39, v39
	v_cvt_f32_f16_sdwa v41, v35 dst_sel:DWORD dst_unused:UNUSED_PAD src0_sel:WORD_1
	v_cvt_f32_f16_e32 v40, v35
	v_sub_f32_e32 v22, v22, v42
	v_sub_f32_e32 v23, v23, v39
	s_waitcnt lgkmcnt(1)
	v_mfma_f32_16x16x32_f16 a[0:3], v[26:29], v[34:37], a[0:3]
	v_add_f32_e64 v24, v24, -v40
	v_add_f32_e64 v25, v25, -v41
	v_cvt_pk_f16_f32 v22, v22, v23
	v_cvt_pk_f16_f32 v23, v24, v25
	v_cvt_f32_f16_sdwa v25, v36 dst_sel:DWORD dst_unused:UNUSED_PAD src0_sel:WORD_1
	v_cvt_f32_f16_e32 v24, v36
	v_cvt_f32_f16_sdwa v41, v37 dst_sel:DWORD dst_unused:UNUSED_PAD src0_sel:WORD_1
	v_cvt_f32_f16_e32 v40, v37
	s_waitcnt lgkmcnt(0)
	v_mfma_f32_16x16x32_f16 a[0:3], v[30:33], v[34:37], a[0:3]
	v_add_f32_e64 v18, v18, -v24
	v_add_f32_e64 v19, v19, -v25
	s_waitcnt vmcnt(2)
	v_cvt_f16_f32_e32 v31, v14
	v_cvt_pk_f16_f32 v24, v18, v19
	v_pk_add_f32 v[18:19], v[20:21], v[40:41] neg_lo:[0,1] neg_hi:[0,1]
	v_cvt_f16_f32_e32 v30, v15
	v_cvt_pk_f16_f32 v25, v18, v19
	v_bitop3_b32 v18, v1, v51, 8 bitop3:0x36
	s_nop 0
	v_mfma_f32_16x16x32_f16 a[0:3], v[26:29], v[22:25], a[0:3]
	v_lshl_or_b32 v22, v18, 4, v38
	ds_read_b128 v[18:21], v22
	ds_read_b128 v[22:25], v22 offset:4096
	v_cvt_pk_f16_f32 v26, v14, v15
	v_cvt_pk_f16_f32 v27, v16, v17
	v_cvt_pk_f16_f32 v28, v10, v11
	v_cvt_pk_f16_f32 v29, v12, v13
	s_and_saveexec_b64 s[4:5], vcc
	s_cbranch_execz .LBB1_8
	global_store_dwordx4 v[48:49], v[26:29], off offset:128 sc1
.LBB1_8:
	s_or_b64 exec, exec, s[4:5]
	v_cvt_f32_f16_e32 v32, v31
	v_cvt_f32_f16_e32 v33, v30
	v_cvt_f32_f16_sdwa v31, v27 dst_sel:DWORD dst_unused:UNUSED_PAD src0_sel:WORD_1
	v_cvt_f32_f16_e32 v30, v27
	v_sub_f32_e32 v14, v14, v32
	v_sub_f32_e32 v15, v15, v33
	s_waitcnt lgkmcnt(1)
	v_mfma_f32_16x16x32_f16 a[0:3], v[18:21], v[26:29], a[0:3]
	v_add_f32_e64 v16, v16, -v30
	v_add_f32_e64 v17, v17, -v31
	v_cvt_pk_f16_f32 v14, v14, v15
	v_cvt_pk_f16_f32 v15, v16, v17
	v_cvt_f32_f16_sdwa v17, v28 dst_sel:DWORD dst_unused:UNUSED_PAD src0_sel:WORD_1
	v_cvt_f32_f16_e32 v16, v28
	v_cvt_f32_f16_sdwa v31, v29 dst_sel:DWORD dst_unused:UNUSED_PAD src0_sel:WORD_1
	v_cvt_f32_f16_e32 v30, v29
	s_waitcnt lgkmcnt(0)
	v_mfma_f32_16x16x32_f16 a[0:3], v[22:25], v[26:29], a[0:3]
	v_add_f32_e64 v10, v10, -v16
	v_add_f32_e64 v11, v11, -v17
	s_waitcnt vmcnt(0)
	v_cvt_f16_f32_e32 v23, v6
	v_cvt_pk_f16_f32 v16, v10, v11
	v_pk_add_f32 v[10:11], v[12:13], v[30:31] neg_lo:[0,1] neg_hi:[0,1]
	v_cvt_f16_f32_e32 v22, v7
	v_cvt_pk_f16_f32 v17, v10, v11
	v_bitop3_b32 v10, v1, v51, 12 bitop3:0x36
	s_nop 0
	v_mfma_f32_16x16x32_f16 a[0:3], v[18:21], v[14:17], a[0:3]
	v_lshl_or_b32 v14, v10, 4, v38
	ds_read_b128 v[10:13], v14
	ds_read_b128 v[14:17], v14 offset:4096
	v_cvt_pk_f16_f32 v18, v6, v7
	v_cvt_pk_f16_f32 v19, v8, v9
	v_cvt_pk_f16_f32 v20, v2, v3
	v_cvt_pk_f16_f32 v21, v4, v5
	s_and_saveexec_b64 s[4:5], vcc
	s_cbranch_execz .LBB1_10
	global_store_dwordx4 v[48:49], v[18:21], off offset:192 sc1
.LBB1_10:
	s_or_b64 exec, exec, s[4:5]
	v_cvt_f32_f16_e32 v24, v23
	v_cvt_f32_f16_e32 v25, v22
	v_cvt_f32_f16_sdwa v23, v19 dst_sel:DWORD dst_unused:UNUSED_PAD src0_sel:WORD_1
	v_cvt_f32_f16_e32 v22, v19
	v_sub_f32_e32 v6, v6, v24
	v_sub_f32_e32 v7, v7, v25
	s_waitcnt lgkmcnt(1)
	v_mfma_f32_16x16x32_f16 a[0:3], v[10:13], v[18:21], a[0:3]
	v_add_f32_e64 v8, v8, -v22
	v_add_f32_e64 v9, v9, -v23
	v_cvt_pk_f16_f32 v6, v6, v7
	v_cvt_pk_f16_f32 v7, v8, v9
	v_cvt_f32_f16_sdwa v9, v20 dst_sel:DWORD dst_unused:UNUSED_PAD src0_sel:WORD_1
	v_cvt_f32_f16_e32 v8, v20
	v_cvt_f32_f16_sdwa v23, v21 dst_sel:DWORD dst_unused:UNUSED_PAD src0_sel:WORD_1
	v_cvt_f32_f16_e32 v22, v21
	s_waitcnt lgkmcnt(0)
	v_mfma_f32_16x16x32_f16 a[0:3], v[14:17], v[18:21], a[0:3]
	v_add_f32_e64 v2, v2, -v8
	v_add_f32_e64 v3, v3, -v9
	v_cmp_gt_u32_e64 s[4:5], 32, v50
	v_cvt_pk_f16_f32 v8, v2, v3
	v_pk_add_f32 v[2:3], v[4:5], v[22:23] neg_lo:[0,1] neg_hi:[0,1]
	s_and_b64 s[4:5], s[4:5], vcc
	v_cvt_pk_f16_f32 v9, v2, v3
	s_nop 1
	v_mfma_f32_16x16x32_f16 a[0:3], v[10:13], v[6:9], a[0:3]
	s_and_b64 exec, exec, s[4:5]
	s_cbranch_execz .LBB1_12
	s_load_dwordx2 s[4:5], s[0:1], 0x60
	s_nop 4
	v_accvgpr_read_b32 v5, a3
	v_lshlrev_b64 v[6:7], 5, v[46:47]
	v_accvgpr_read_b32 v4, a2
	v_accvgpr_read_b32 v3, a1
	v_accvgpr_read_b32 v2, a0
	v_lshlrev_b32_e32 v8, 4, v1
	v_mov_b32_e32 v9, 0
	s_waitcnt lgkmcnt(0)
	v_lshl_add_u64 v[6:7], s[4:5], 0, v[6:7]
	s_mov_b32 s4, 0x3fb8aa3b
	v_lshl_add_u64 v[6:7], v[6:7], 0, v[8:9]
	v_pk_mul_f32 v[2:3], v[2:3], s[4:5] op_sel_hi:[1,0]
	v_pk_mul_f32 v[4:5], v[4:5], s[4:5] op_sel_hi:[1,0]
	global_store_dwordx4 v[6:7], v[2:5], off sc1

.Lp1_entry:
	s_load_dwordx4 s[4:7], s[0:1], 0x0
	s_load_dwordx2 s[8:9], s[0:1], 0x20
	s_load_dwordx2 s[10:11], s[0:1], 0x28
	s_load_dwordx2 s[12:13], s[0:1], 0x50
	v_lshlrev_b32_e32 v1, 4, v0
	v_mov_b32_e32 v2, 0
	v_mov_b32_e32 v3, 0
	v_mov_b32_e32 v4, 0
	v_mov_b32_e32 v5, 0
	ds_write_b128 v1, v[2:5]
	s_mul_i32 s3, s2, 0x180
	v_add_u32_e32 v4, s3, v0
	v_add_u32_e32 v5, 0x80, v4
	v_add_u32_e32 v6, 0x100, v4
	s_mov_b32 s14, 0x30d40
	v_cmp_gt_u32_e64 s[16:17], s14, v4
	v_cmp_gt_u32_e64 s[18:19], s14, v5
	v_cmp_gt_u32_e64 s[20:21], s14, v6
	v_min_u32_e32 v4, 0x30d3f, v4
	v_min_u32_e32 v5, 0x30d3f, v5
	v_min_u32_e32 v6, 0x30d3f, v6
	v_lshlrev_b32_e32 v4, 4, v4
	v_lshlrev_b32_e32 v5, 4, v5
	v_lshlrev_b32_e32 v6, 4, v6
	s_waitcnt lgkmcnt(0)
	s_add_u32 s14, s4, 0x30d400
	s_addc_u32 s15, s5, 0
	global_load_dwordx4 v[8:11], v4, s[6:7] nt
	global_load_dwordx4 v[12:15], v4, s[4:5] nt
	global_load_dwordx4 v[16:19], v4, s[14:15] nt
	global_load_dwordx4 v[20:23], v5, s[6:7] nt
	global_load_dwordx4 v[24:27], v5, s[4:5] nt
	global_load_dwordx4 v[28:31], v5, s[14:15] nt
	global_load_dwordx4 v[32:35], v6, s[6:7] nt
	global_load_dwordx4 v[36:39], v6, s[4:5] nt
	global_load_dwordx4 v[40:43], v6, s[14:15] nt
	v_mov_b32_e32 v48, 1
	s_mov_b32 s31, 0
	s_mov_b32 s30, 0xc350
	s_barrier
	s_waitcnt vmcnt(6)
	v_mul_lo_u32 v44, v12, v8
	v_mul_lo_u32 v45, v16, v8
	v_cmp_ne_u32_e64 s[22:23], 0, v8
	v_max_u32_e32 v46, v44, v45
	v_cmp_gt_u32_e32 vcc, s30, v46
	s_and_b64 vcc, vcc, s[22:23]
	s_and_b64 vcc, vcc, s[16:17]
	s_andn2_b64 s[24:25], s[16:17], s[22:23]
	s_bcnt1_i32_b64 s26, s[24:25]
	s_add_i32 s31, s31, s26
	v_lshl_or_b32 v12, v45, 16, v44
	v_cndmask_b32_e32 v12, -1, v12, vcc
	v_lshrrev_b32_e32 v47, 21, v12
	v_and_b32_e32 v47, 0x7fc, v47
	ds_add_rtn_u32 v16, v47, v48
	v_mul_lo_u32 v44, v13, v9
	v_mul_lo_u32 v45, v17, v9
	v_cmp_ne_u32_e64 s[22:23], 0, v9
	v_max_u32_e32 v46, v44, v45
	v_cmp_gt_u32_e32 vcc, s30, v46
	s_and_b64 vcc, vcc, s[22:23]
	s_and_b64 vcc, vcc, s[16:17]
	s_andn2_b64 s[24:25], s[16:17], s[22:23]
	s_bcnt1_i32_b64 s26, s[24:25]
	s_add_i32 s31, s31, s26
	v_lshl_or_b32 v13, v45, 16, v44
	v_cndmask_b32_e32 v13, -1, v13, vcc
	v_lshrrev_b32_e32 v47, 21, v13
	v_and_b32_e32 v47, 0x7fc, v47
	ds_add_rtn_u32 v17, v47, v48
	v_mul_lo_u32 v44, v14, v10
	v_mul_lo_u32 v45, v18, v10
	v_cmp_ne_u32_e64 s[22:23], 0, v10
	v_max_u32_e32 v46, v44, v45
	v_cmp_gt_u32_e32 vcc, s30, v46
	s_and_b64 vcc, vcc, s[22:23]
	s_and_b64 vcc, vcc, s[16:17]
	s_andn2_b64 s[24:25], s[16:17], s[22:23]
	s_bcnt1_i32_b64 s26, s[24:25]
	s_add_i32 s31, s31, s26
	v_lshl_or_b32 v14, v45, 16, v44
	v_cndmask_b32_e32 v14, -1, v14, vcc
	v_lshrrev_b32_e32 v47, 21, v14
	v_and_b32_e32 v47, 0x7fc, v47
	ds_add_rtn_u32 v18, v47, v48
	v_mul_lo_u32 v44, v15, v11
	v_mul_lo_u32 v45, v19, v11
	v_cmp_ne_u32_e64 s[22:23], 0, v11
	v_max_u32_e32 v46, v44, v45
	v_cmp_gt_u32_e32 vcc, s30, v46
	s_and_b64 vcc, vcc, s[22:23]
	s_and_b64 vcc, vcc, s[16:17]
	s_andn2_b64 s[24:25], s[16:17], s[22:23]
	s_bcnt1_i32_b64 s26, s[24:25]
	s_add_i32 s31, s31, s26
	v_lshl_or_b32 v15, v45, 16, v44
	v_cndmask_b32_e32 v15, -1, v15, vcc
	v_lshrrev_b32_e32 v47, 21, v15
	v_and_b32_e32 v47, 0x7fc, v47
	ds_add_rtn_u32 v19, v47, v48
	s_waitcnt vmcnt(3)
	v_mul_lo_u32 v44, v24, v20
	v_mul_lo_u32 v45, v28, v20
	v_cmp_ne_u32_e64 s[22:23], 0, v20
	v_max_u32_e32 v46, v44, v45
	v_cmp_gt_u32_e32 vcc, s30, v46
	s_and_b64 vcc, vcc, s[22:23]
	s_and_b64 vcc, vcc, s[18:19]
	s_andn2_b64 s[24:25], s[18:19], s[22:23]
	s_bcnt1_i32_b64 s26, s[24:25]
	s_add_i32 s31, s31, s26
	v_lshl_or_b32 v24, v45, 16, v44
	v_cndmask_b32_e32 v24, -1, v24, vcc
	v_lshrrev_b32_e32 v47, 21, v24
	v_and_b32_e32 v47, 0x7fc, v47
	ds_add_rtn_u32 v28, v47, v48
	v_mul_lo_u32 v44, v25, v21
	v_mul_lo_u32 v45, v29, v21
	v_cmp_ne_u32_e64 s[22:23], 0, v21
	v_max_u32_e32 v46, v44, v45
	v_cmp_gt_u32_e32 vcc, s30, v46
	s_and_b64 vcc, vcc, s[22:23]
	s_and_b64 vcc, vcc, s[18:19]
	s_andn2_b64 s[24:25], s[18:19], s[22:23]
	s_bcnt1_i32_b64 s26, s[24:25]
	s_add_i32 s31, s31, s26
	v_lshl_or_b32 v25, v45, 16, v44
	v_cndmask_b32_e32 v25, -1, v25, vcc
	v_lshrrev_b32_e32 v47, 21, v25
	v_and_b32_e32 v47, 0x7fc, v47
	ds_add_rtn_u32 v29, v47, v48
	v_mul_lo_u32 v44, v26, v22
	v_mul_lo_u32 v45, v30, v22
	v_cmp_ne_u32_e64 s[22:23], 0, v22
	v_max_u32_e32 v46, v44, v45
	v_cmp_gt_u32_e32 vcc, s30, v46
	s_and_b64 vcc, vcc, s[22:23]
	s_and_b64 vcc, vcc, s[18:19]
	s_andn2_b64 s[24:25], s[18:19], s[22:23]
	s_bcnt1_i32_b64 s26, s[24:25]
	s_add_i32 s31, s31, s26
	v_lshl_or_b32 v26, v45, 16, v44
	v_cndmask_b32_e32 v26, -1, v26, vcc
	v_lshrrev_b32_e32 v47, 21, v26
	v_and_b32_e32 v47, 0x7fc, v47
	ds_add_rtn_u32 v30, v47, v48
	v_mul_lo_u32 v44, v27, v23
	v_mul_lo_u32 v45, v31, v23
	v_cmp_ne_u32_e64 s[22:23], 0, v23
	v_max_u32_e32 v46, v44, v45
	v_cmp_gt_u32_e32 vcc, s30, v46
	s_and_b64 vcc, vcc, s[22:23]
	s_and_b64 vcc, vcc, s[18:19]
	s_andn2_b64 s[24:25], s[18:19], s[22:23]
	s_bcnt1_i32_b64 s26, s[24:25]
	s_add_i32 s31, s31, s26
	v_lshl_or_b32 v27, v45, 16, v44
	v_cndmask_b32_e32 v27, -1, v27, vcc
	v_lshrrev_b32_e32 v47, 21, v27
	v_and_b32_e32 v47, 0x7fc, v47
	ds_add_rtn_u32 v31, v47, v48
	s_waitcnt vmcnt(0)
	v_mul_lo_u32 v44, v36, v32
	v_mul_lo_u32 v45, v40, v32
	v_cmp_ne_u32_e64 s[22:23], 0, v32
	v_max_u32_e32 v46, v44, v45
	v_cmp_gt_u32_e32 vcc, s30, v46
	s_and_b64 vcc, vcc, s[22:23]
	s_and_b64 vcc, vcc, s[20:21]
	s_andn2_b64 s[24:25], s[20:21], s[22:23]
	s_bcnt1_i32_b64 s26, s[24:25]
	s_add_i32 s31, s31, s26
	v_lshl_or_b32 v36, v45, 16, v44
	v_cndmask_b32_e32 v36, -1, v36, vcc
	v_lshrrev_b32_e32 v47, 21, v36
	v_and_b32_e32 v47, 0x7fc, v47
	ds_add_rtn_u32 v40, v47, v48
	v_mul_lo_u32 v44, v37, v33
	v_mul_lo_u32 v45, v41, v33
	v_cmp_ne_u32_e64 s[22:23], 0, v33
	v_max_u32_e32 v46, v44, v45
	v_cmp_gt_u32_e32 vcc, s30, v46
	s_and_b64 vcc, vcc, s[22:23]
	s_and_b64 vcc, vcc, s[20:21]
	s_andn2_b64 s[24:25], s[20:21], s[22:23]
	s_bcnt1_i32_b64 s26, s[24:25]
	s_add_i32 s31, s31, s26
	v_lshl_or_b32 v37, v45, 16, v44
	v_cndmask_b32_e32 v37, -1, v37, vcc
	v_lshrrev_b32_e32 v47, 21, v37
	v_and_b32_e32 v47, 0x7fc, v47
	ds_add_rtn_u32 v41, v47, v48
	v_mul_lo_u32 v44, v38, v34
	v_mul_lo_u32 v45, v42, v34
	v_cmp_ne_u32_e64 s[22:23], 0, v34
	v_max_u32_e32 v46, v44, v45
	v_cmp_gt_u32_e32 vcc, s30, v46
	s_and_b64 vcc, vcc, s[22:23]
	s_and_b64 vcc, vcc, s[20:21]
	s_andn2_b64 s[24:25], s[20:21], s[22:23]
	s_bcnt1_i32_b64 s26, s[24:25]
	s_add_i32 s31, s31, s26
	v_lshl_or_b32 v38, v45, 16, v44
	v_cndmask_b32_e32 v38, -1, v38, vcc
	v_lshrrev_b32_e32 v47, 21, v38
	v_and_b32_e32 v47, 0x7fc, v47
	ds_add_rtn_u32 v42, v47, v48
	v_mul_lo_u32 v44, v39, v35
	v_mul_lo_u32 v45, v43, v35
	v_cmp_ne_u32_e64 s[22:23], 0, v35
	v_max_u32_e32 v46, v44, v45
	v_cmp_gt_u32_e32 vcc, s30, v46
	s_and_b64 vcc, vcc, s[22:23]
	s_and_b64 vcc, vcc, s[20:21]
	s_andn2_b64 s[24:25], s[20:21], s[22:23]
	s_bcnt1_i32_b64 s26, s[24:25]
	s_add_i32 s31, s31, s26
	v_lshl_or_b32 v39, v45, 16, v44
	v_cndmask_b32_e32 v39, -1, v39, vcc
	v_lshrrev_b32_e32 v47, 21, v39
	v_and_b32_e32 v47, 0x7fc, v47
	ds_add_rtn_u32 v43, v47, v48
	s_waitcnt lgkmcnt(0)
	s_barrier
	v_readfirstlane_b32 s3, v0
	s_cmp_lt_u32 s3, 64
	s_cbranch_scc0 .Lp1_scan_done
	v_lshlrev_b32_e32 v1, 5, v0
	ds_read_b128 v[8:11], v1 offset:0
	ds_read_b128 v[20:23], v1 offset:16
	v_mov_b32_e32 v44, 0
	s_waitcnt lgkmcnt(0)
	v_mov_b32_e32 v54, v44
	v_add_u32_e32 v44, v44, v8
	v_mov_b32_e32 v55, v44
	v_add_u32_e32 v44, v44, v9
	v_mov_b32_e32 v56, v44
	v_add_u32_e32 v44, v44, v10
	v_mov_b32_e32 v57, v44
	v_add_u32_e32 v44, v44, v11
	v_mov_b32_e32 v58, v44
	v_add_u32_e32 v44, v44, v20
	v_mov_b32_e32 v59, v44
	v_add_u32_e32 v44, v44, v21
	v_mov_b32_e32 v60, v44
	v_add_u32_e32 v44, v44, v22
	v_mov_b32_e32 v61, v44
	v_add_u32_e32 v44, v44, v23
	v_mov_b32_e32 v45, v44
	s_nop 1
	v_add_u32_dpp v45, v45, v45 row_shr:1 row_mask:0xf bank_mask:0xf bound_ctrl:1
	s_nop 1
	v_add_u32_dpp v45, v45, v45 row_shr:2 row_mask:0xf bank_mask:0xf bound_ctrl:1
	s_nop 1
	v_add_u32_dpp v45, v45, v45 row_shr:4 row_mask:0xf bank_mask:0xf bound_ctrl:1
	s_nop 1
	v_add_u32_dpp v45, v45, v45 row_shr:8 row_mask:0xf bank_mask:0xf bound_ctrl:1
	s_nop 1
	v_add_u32_dpp v45, v45, v45 row_bcast:15 row_mask:0xa bank_mask:0xf
	s_nop 1
	v_add_u32_dpp v45, v45, v45 row_bcast:31 row_mask:0xc bank_mask:0xf
	s_nop 1
	v_sub_u32_e32 v46, v45, v44
	v_add_u32_e32 v54, v54, v46
	v_add_u32_e32 v55, v55, v46
	v_add_u32_e32 v56, v56, v46
	v_add_u32_e32 v57, v57, v46
	v_add_u32_e32 v58, v58, v46
	v_add_u32_e32 v59, v59, v46
	v_add_u32_e32 v60, v60, v46
	v_add_u32_e32 v61, v61, v46
	ds_write_b128 v1, v[54:57] offset:0
	ds_write_b128 v1, v[58:61] offset:16
	v_lshl_or_b32 v8, v8, 16, v54
	v_lshl_or_b32 v9, v9, 16, v55
	v_lshl_or_b32 v10, v10, 16, v56
	v_lshl_or_b32 v11, v11, 16, v57
	v_lshl_or_b32 v20, v20, 16, v58
	v_lshl_or_b32 v21, v21, 16, v59
	v_lshl_or_b32 v22, v22, 16, v60
	v_lshl_or_b32 v23, v23, 16, v61
	s_mul_i32 s3, s2, 0x880
	s_add_u32 s24, s12, 0x41a000
	s_addc_u32 s25, s13, 0
	s_add_u32 s24, s24, s3
	s_addc_u32 s25, s25, 0
	global_store_dwordx4 v1, v[8:11], s[24:25] offset:0 sc1
	global_store_dwordx4 v1, v[20:23], s[24:25] offset:16 sc1

.Lp2_polled:
	s_barrier
	v_mul_u32_u24_e32 v13, 0x880, v0
	global_load_dword v2, v13, s[24:25] sc1
	v_add_u32_e32 v14, 0x44000, v13
	global_load_dword v3, v14, s[24:25] sc1
	v_add_u32_e32 v14, 0x88000, v13
	global_load_dword v4, v14, s[24:25] sc1
	v_add_u32_e32 v14, 0xcc000, v13
	global_load_dword v5, v14, s[24:25] sc1
	v_add_u32_e32 v14, 0x110000, v13
	v_mov_b32_e32 v6, 0
	v_cmp_gt_u32_e32 vcc, 9, v0
	s_and_saveexec_b64 s[22:23], vcc
	global_load_dword v6, v14, s[24:25] sc1
	s_mov_b64 exec, s[22:23]
	v_mul_u32_u24_e32 v13, 0x1800, v0
	s_waitcnt vmcnt(0)
	v_lshrrev_b32_e32 v7, 16, v2
	v_and_b32_e32 v2, 0xffff, v2
	v_lshl_add_u32 v2, v2, 2, v13
	v_lshrrev_b32_e32 v8, 16, v3
	v_and_b32_e32 v3, 0xffff, v3
	v_add_u32_e32 v14, 0xc0000, v13
	v_lshl_add_u32 v3, v3, 2, v14
	v_lshrrev_b32_e32 v9, 16, v4
	v_and_b32_e32 v4, 0xffff, v4
	v_add_u32_e32 v14, 0x180000, v13
	v_lshl_add_u32 v4, v4, 2, v14
	v_lshrrev_b32_e32 v10, 16, v5
	v_and_b32_e32 v5, 0xffff, v5
	v_add_u32_e32 v14, 0x240000, v13
	v_lshl_add_u32 v5, v5, 2, v14
	v_lshrrev_b32_e32 v11, 16, v6
	v_and_b32_e32 v6, 0xffff, v6
	v_add_u32_e32 v14, 0x300000, v13
	v_lshl_add_u32 v6, v6, 2, v14
	v_cmp_lt_u32_e32 vcc, 0, v7
	s_and_saveexec_b64 s[22:23], vcc
	global_load_dwordx4 v[20:23], v2, s[26:27] sc1
	v_cmp_lt_u32_e32 vcc, 4, v7
	s_and_b64 exec, exec, vcc
	global_load_dwordx4 v[24:27], v2, s[26:27] offset:16 sc1
	s_mov_b64 exec, s[22:23]
	v_cmp_lt_u32_e32 vcc, 0, v8
	s_and_saveexec_b64 s[22:23], vcc
	global_load_dwordx4 v[28:31], v3, s[26:27] sc1
	v_cmp_lt_u32_e32 vcc, 4, v8
	s_and_b64 exec, exec, vcc
	global_load_dwordx4 v[32:35], v3, s[26:27] offset:16 sc1
	s_mov_b64 exec, s[22:23]
	v_cmp_lt_u32_e32 vcc, 0, v9
	s_and_saveexec_b64 s[22:23], vcc
	global_load_dwordx4 v[36:39], v4, s[26:27] sc1
	v_cmp_lt_u32_e32 vcc, 4, v9
	s_and_b64 exec, exec, vcc
	global_load_dwordx4 v[40:43], v4, s[26:27] offset:16 sc1
	s_mov_b64 exec, s[22:23]
	v_cmp_lt_u32_e32 vcc, 0, v10
	s_and_saveexec_b64 s[22:23], vcc
	global_load_dwordx4 v[44:47], v5, s[26:27] sc1
	v_cmp_lt_u32_e32 vcc, 4, v10
	s_and_b64 exec, exec, vcc
	global_load_dwordx4 v[48:51], v5, s[26:27] offset:16 sc1
	s_mov_b64 exec, s[22:23]
	v_cmp_lt_u32_e32 vcc, 0, v11
	s_and_saveexec_b64 s[22:23], vcc
	global_load_dwordx4 v[52:55], v6, s[26:27] sc1
	v_cmp_lt_u32_e32 vcc, 4, v11
	s_and_b64 exec, exec, vcc
	global_load_dwordx4 v[56:59], v6, s[26:27] offset:16 sc1
	s_mov_b64 exec, s[22:23]
	s_waitcnt vmcnt(0)
	v_cmp_lt_u32_e32 vcc, 0, v7
	s_cbranch_vccz .Lp2_c0_p1done
	s_and_saveexec_b64 s[22:23], vcc
	v_bfe_u32 v13, v20, 16, 7
	v_lshlrev_b32_e32 v13, 2, v13
	ds_add_rtn_u32 v60, v13, v12
	s_mov_b64 exec, s[22:23]
	v_cmp_lt_u32_e32 vcc, 1, v7
	s_cbranch_vccz .Lp2_c0_p1done
	s_and_saveexec_b64 s[22:23], vcc
	v_bfe_u32 v13, v21, 16, 7
	v_lshlrev_b32_e32 v13, 2, v13
	ds_add_rtn_u32 v61, v13, v12
	s_mov_b64 exec, s[22:23]
	v_cmp_lt_u32_e32 vcc, 2, v7
	s_cbranch_vccz .Lp2_c0_p1done
	s_and_saveexec_b64 s[22:23], vcc
	v_bfe_u32 v13, v22, 16, 7
	v_lshlrev_b32_e32 v13, 2, v13
	ds_add_rtn_u32 v62, v13, v12
	s_mov_b64 exec, s[22:23]
	v_cmp_lt_u32_e32 vcc, 3, v7
	s_cbranch_vccz .Lp2_c0_p1done
	s_and_saveexec_b64 s[22:23], vcc
	v_bfe_u32 v13, v23, 16, 7
	v_lshlrev_b32_e32 v13, 2, v13
	ds_add_rtn_u32 v63, v13, v12
	s_mov_b64 exec, s[22:23]
	v_cmp_lt_u32_e32 vcc, 4, v7
	s_cbranch_vccz .Lp2_c0_p1done
	s_and_saveexec_b64 s[22:23], vcc
	v_bfe_u32 v13, v24, 16, 7
	v_lshlrev_b32_e32 v13, 2, v13
	ds_add_rtn_u32 v64, v13, v12
	s_mov_b64 exec, s[22:23]
	v_cmp_lt_u32_e32 vcc, 5, v7
	s_cbranch_vccz .Lp2_c0_p1done
	s_and_saveexec_b64 s[22:23], vcc
	v_bfe_u32 v13, v25, 16, 7
	v_lshlrev_b32_e32 v13, 2, v13
	ds_add_rtn_u32 v65, v13, v12
	s_mov_b64 exec, s[22:23]
	v_cmp_lt_u32_e32 vcc, 6, v7
	s_cbranch_vccz .Lp2_c0_p1done
	s_and_saveexec_b64 s[22:23], vcc
	v_bfe_u32 v13, v26, 16, 7
	v_lshlrev_b32_e32 v13, 2, v13
	ds_add_rtn_u32 v66, v13, v12
	s_mov_b64 exec, s[22:23]
	v_cmp_lt_u32_e32 vcc, 7, v7
	s_cbranch_vccz .Lp2_c0_p1done
	s_and_saveexec_b64 s[22:23], vcc
	v_bfe_u32 v13, v27, 16, 7
	v_lshlrev_b32_e32 v13, 2, v13
	ds_add_rtn_u32 v67, v13, v12
	s_mov_b64 exec, s[22:23]

.Lp2_c3_p1done:
	s_waitcnt lgkmcnt(0)
	v_cmp_lt_u32_e32 vcc, 0, v7
	s_cbranch_vccz .Lp2_c0_p2done
	s_and_saveexec_b64 s[22:23], vcc
	v_cmp_gt_u32_e32 vcc, 32, v60
	s_andn2_b64 s[36:37], exec, vcc
	s_or_b64 s[38:39], s[38:39], s[36:37]
	s_and_b64 exec, exec, vcc
	v_lshrrev_b32_e32 v13, 16, v20
	v_lshl_add_u32 v13, v13, 5, v60
	v_lshlrev_b32_e32 v13, 2, v13
	v_and_b32_e32 v14, 0xffff, v20
	global_store_dword v13, v14, s[6:7] sc1
	s_mov_b64 exec, s[22:23]
	v_cmp_lt_u32_e32 vcc, 1, v7
	s_cbranch_vccz .Lp2_c0_p2done
	s_and_saveexec_b64 s[22:23], vcc
	v_cmp_gt_u32_e32 vcc, 32, v61
	s_andn2_b64 s[36:37], exec, vcc
	s_or_b64 s[38:39], s[38:39], s[36:37]
	s_and_b64 exec, exec, vcc
	v_lshrrev_b32_e32 v13, 16, v21
	v_lshl_add_u32 v13, v13, 5, v61
	v_lshlrev_b32_e32 v13, 2, v13
	v_and_b32_e32 v14, 0xffff, v21
	global_store_dword v13, v14, s[6:7] sc1
	s_mov_b64 exec, s[22:23]
	v_cmp_lt_u32_e32 vcc, 2, v7
	s_cbranch_vccz .Lp2_c0_p2done
	s_and_saveexec_b64 s[22:23], vcc
	v_cmp_gt_u32_e32 vcc, 32, v62
	s_andn2_b64 s[36:37], exec, vcc
	s_or_b64 s[38:39], s[38:39], s[36:37]
	s_and_b64 exec, exec, vcc
	v_lshrrev_b32_e32 v13, 16, v22
	v_lshl_add_u32 v13, v13, 5, v62
	v_lshlrev_b32_e32 v13, 2, v13
	v_and_b32_e32 v14, 0xffff, v22
	global_store_dword v13, v14, s[6:7] sc1
	s_mov_b64 exec, s[22:23]
	v_cmp_lt_u32_e32 vcc, 3, v7
	s_cbranch_vccz .Lp2_c0_p2done
	s_and_saveexec_b64 s[22:23], vcc
	v_cmp_gt_u32_e32 vcc, 32, v63
	s_andn2_b64 s[36:37], exec, vcc
	s_or_b64 s[38:39], s[38:39], s[36:37]
	s_and_b64 exec, exec, vcc
	v_lshrrev_b32_e32 v13, 16, v23
	v_lshl_add_u32 v13, v13, 5, v63
	v_lshlrev_b32_e32 v13, 2, v13
	v_and_b32_e32 v14, 0xffff, v23
	global_store_dword v13, v14, s[6:7] sc1
	s_mov_b64 exec, s[22:23]
	v_cmp_lt_u32_e32 vcc, 4, v7
	s_cbranch_vccz .Lp2_c0_p2done
	s_and_saveexec_b64 s[22:23], vcc
	v_cmp_gt_u32_e32 vcc, 32, v64
	s_andn2_b64 s[36:37], exec, vcc
	s_or_b64 s[38:39], s[38:39], s[36:37]
	s_and_b64 exec, exec, vcc
	v_lshrrev_b32_e32 v13, 16, v24
	v_lshl_add_u32 v13, v13, 5, v64
	v_lshlrev_b32_e32 v13, 2, v13
	v_and_b32_e32 v14, 0xffff, v24
	global_store_dword v13, v14, s[6:7] sc1
	s_mov_b64 exec, s[22:23]
	v_cmp_lt_u32_e32 vcc, 5, v7
	s_cbranch_vccz .Lp2_c0_p2done
	s_and_saveexec_b64 s[22:23], vcc
	v_cmp_gt_u32_e32 vcc, 32, v65
	s_andn2_b64 s[36:37], exec, vcc
	s_or_b64 s[38:39], s[38:39], s[36:37]
	s_and_b64 exec, exec, vcc
	v_lshrrev_b32_e32 v13, 16, v25
	v_lshl_add_u32 v13, v13, 5, v65
	v_lshlrev_b32_e32 v13, 2, v13
	v_and_b32_e32 v14, 0xffff, v25
	global_store_dword v13, v14, s[6:7] sc1
	s_mov_b64 exec, s[22:23]
	v_cmp_lt_u32_e32 vcc, 6, v7
	s_cbranch_vccz .Lp2_c0_p2done
	s_and_saveexec_b64 s[22:23], vcc
	v_cmp_gt_u32_e32 vcc, 32, v66
	s_andn2_b64 s[36:37], exec, vcc
	s_or_b64 s[38:39], s[38:39], s[36:37]
	s_and_b64 exec, exec, vcc
	v_lshrrev_b32_e32 v13, 16, v26
	v_lshl_add_u32 v13, v13, 5, v66
	v_lshlrev_b32_e32 v13, 2, v13
	v_and_b32_e32 v14, 0xffff, v26
	global_store_dword v13, v14, s[6:7] sc1
	s_mov_b64 exec, s[22:23]
	v_cmp_lt_u32_e32 vcc, 7, v7
	s_cbranch_vccz .Lp2_c0_p2done
	s_and_saveexec_b64 s[22:23], vcc
	v_cmp_gt_u32_e32 vcc, 32, v67
	s_andn2_b64 s[36:37], exec, vcc
	s_or_b64 s[38:39], s[38:39], s[36:37]
	s_and_b64 exec, exec, vcc
	v_lshrrev_b32_e32 v13, 16, v27
	v_lshl_add_u32 v13, v13, 5, v67
	v_lshlrev_b32_e32 v13, 2, v13
	v_and_b32_e32 v14, 0xffff, v27
	global_store_dword v13, v14, s[6:7] sc1
	s_mov_b64 exec, s[22:23]
.Lp2_c0_p2done:
	v_cmp_lt_u32_e32 vcc, 0, v8
	s_cbranch_vccz .Lp2_c1_p2done
	s_and_saveexec_b64 s[22:23], vcc
	v_cmp_gt_u32_e32 vcc, 32, v68
	s_andn2_b64 s[36:37], exec, vcc
	s_or_b64 s[38:39], s[38:39], s[36:37]
	s_and_b64 exec, exec, vcc
	v_lshrrev_b32_e32 v13, 16, v28
	v_lshl_add_u32 v13, v13, 5, v68
	v_lshlrev_b32_e32 v13, 2, v13
	v_and_b32_e32 v14, 0xffff, v28
	global_store_dword v13, v14, s[6:7] sc1
	s_mov_b64 exec, s[22:23]
	v_cmp_lt_u32_e32 vcc, 1, v8
	s_cbranch_vccz .Lp2_c1_p2done
	s_and_saveexec_b64 s[22:23], vcc
	v_cmp_gt_u32_e32 vcc, 32, v69
	s_andn2_b64 s[36:37], exec, vcc
	s_or_b64 s[38:39], s[38:39], s[36:37]
	s_and_b64 exec, exec, vcc
	v_lshrrev_b32_e32 v13, 16, v29
	v_lshl_add_u32 v13, v13, 5, v69
	v_lshlrev_b32_e32 v13, 2, v13
	v_and_b32_e32 v14, 0xffff, v29
	global_store_dword v13, v14, s[6:7] sc1
	s_mov_b64 exec, s[22:23]
	v_cmp_lt_u32_e32 vcc, 2, v8
	s_cbranch_vccz .Lp2_c1_p2done
	s_and_saveexec_b64 s[22:23], vcc
	v_cmp_gt_u32_e32 vcc, 32, v70
	s_andn2_b64 s[36:37], exec, vcc
	s_or_b64 s[38:39], s[38:39], s[36:37]
	s_and_b64 exec, exec, vcc
	v_lshrrev_b32_e32 v13, 16, v30
	v_lshl_add_u32 v13, v13, 5, v70
	v_lshlrev_b32_e32 v13, 2, v13
	v_and_b32_e32 v14, 0xffff, v30
	global_store_dword v13, v14, s[6:7] sc1
	s_mov_b64 exec, s[22:23]
	v_cmp_lt_u32_e32 vcc, 3, v8
	s_cbranch_vccz .Lp2_c1_p2done
	s_and_saveexec_b64 s[22:23], vcc
	v_cmp_gt_u32_e32 vcc, 32, v71
	s_andn2_b64 s[36:37], exec, vcc
	s_or_b64 s[38:39], s[38:39], s[36:37]
	s_and_b64 exec, exec, vcc
	v_lshrrev_b32_e32 v13, 16, v31
	v_lshl_add_u32 v13, v13, 5, v71
	v_lshlrev_b32_e32 v13, 2, v13
	v_and_b32_e32 v14, 0xffff, v31
	global_store_dword v13, v14, s[6:7] sc1
	s_mov_b64 exec, s[22:23]
	v_cmp_lt_u32_e32 vcc, 4, v8
	s_cbranch_vccz .Lp2_c1_p2done
	s_and_saveexec_b64 s[22:23], vcc
	v_cmp_gt_u32_e32 vcc, 32, v72
	s_andn2_b64 s[36:37], exec, vcc
	s_or_b64 s[38:39], s[38:39], s[36:37]
	s_and_b64 exec, exec, vcc
	v_lshrrev_b32_e32 v13, 16, v32
	v_lshl_add_u32 v13, v13, 5, v72
	v_lshlrev_b32_e32 v13, 2, v13
	v_and_b32_e32 v14, 0xffff, v32
	global_store_dword v13, v14, s[6:7] sc1
	s_mov_b64 exec, s[22:23]
	v_cmp_lt_u32_e32 vcc, 5, v8
	s_cbranch_vccz .Lp2_c1_p2done
	s_and_saveexec_b64 s[22:23], vcc
	v_cmp_gt_u32_e32 vcc, 32, v73
	s_andn2_b64 s[36:37], exec, vcc
	s_or_b64 s[38:39], s[38:39], s[36:37]
	s_and_b64 exec, exec, vcc
	v_lshrrev_b32_e32 v13, 16, v33
	v_lshl_add_u32 v13, v13, 5, v73
	v_lshlrev_b32_e32 v13, 2, v13
	v_and_b32_e32 v14, 0xffff, v33
	global_store_dword v13, v14, s[6:7] sc1
	s_mov_b64 exec, s[22:23]
	v_cmp_lt_u32_e32 vcc, 6, v8
	s_cbranch_vccz .Lp2_c1_p2done
	s_and_saveexec_b64 s[22:23], vcc
	v_cmp_gt_u32_e32 vcc, 32, v74
	s_andn2_b64 s[36:37], exec, vcc
	s_or_b64 s[38:39], s[38:39], s[36:37]
	s_and_b64 exec, exec, vcc
	v_lshrrev_b32_e32 v13, 16, v34
	v_lshl_add_u32 v13, v13, 5, v74
	v_lshlrev_b32_e32 v13, 2, v13
	v_and_b32_e32 v14, 0xffff, v34
	global_store_dword v13, v14, s[6:7] sc1
	s_mov_b64 exec, s[22:23]
	v_cmp_lt_u32_e32 vcc, 7, v8
	s_cbranch_vccz .Lp2_c1_p2done
	s_and_saveexec_b64 s[22:23], vcc
	v_cmp_gt_u32_e32 vcc, 32, v75
	s_andn2_b64 s[36:37], exec, vcc
	s_or_b64 s[38:39], s[38:39], s[36:37]
	s_and_b64 exec, exec, vcc
	v_lshrrev_b32_e32 v13, 16, v35
	v_lshl_add_u32 v13, v13, 5, v75
	v_lshlrev_b32_e32 v13, 2, v13
	v_and_b32_e32 v14, 0xffff, v35
	global_store_dword v13, v14, s[6:7] sc1
	s_mov_b64 exec, s[22:23]
.Lp2_c1_p2done:
	v_cmp_lt_u32_e32 vcc, 0, v9
	s_cbranch_vccz .Lp2_c2_p2done
	s_and_saveexec_b64 s[22:23], vcc
	v_cmp_gt_u32_e32 vcc, 32, v76
	s_andn2_b64 s[36:37], exec, vcc
	s_or_b64 s[38:39], s[38:39], s[36:37]
	s_and_b64 exec, exec, vcc
	v_lshrrev_b32_e32 v13, 16, v36
	v_lshl_add_u32 v13, v13, 5, v76
	v_lshlrev_b32_e32 v13, 2, v13
	v_and_b32_e32 v14, 0xffff, v36
	global_store_dword v13, v14, s[6:7] sc1
	s_mov_b64 exec, s[22:23]
	v_cmp_lt_u32_e32 vcc, 1, v9
	s_cbranch_vccz .Lp2_c2_p2done
	s_and_saveexec_b64 s[22:23], vcc
	v_cmp_gt_u32_e32 vcc, 32, v77
	s_andn2_b64 s[36:37], exec, vcc
	s_or_b64 s[38:39], s[38:39], s[36:37]
	s_and_b64 exec, exec, vcc
	v_lshrrev_b32_e32 v13, 16, v37
	v_lshl_add_u32 v13, v13, 5, v77
	v_lshlrev_b32_e32 v13, 2, v13
	v_and_b32_e32 v14, 0xffff, v37
	global_store_dword v13, v14, s[6:7] sc1
	s_mov_b64 exec, s[22:23]
	v_cmp_lt_u32_e32 vcc, 2, v9
	s_cbranch_vccz .Lp2_c2_p2done
	s_and_saveexec_b64 s[22:23], vcc
	v_cmp_gt_u32_e32 vcc, 32, v78
	s_andn2_b64 s[36:37], exec, vcc
	s_or_b64 s[38:39], s[38:39], s[36:37]
	s_and_b64 exec, exec, vcc
	v_lshrrev_b32_e32 v13, 16, v38
	v_lshl_add_u32 v13, v13, 5, v78
	v_lshlrev_b32_e32 v13, 2, v13
	v_and_b32_e32 v14, 0xffff, v38
	global_store_dword v13, v14, s[6:7] sc1
	s_mov_b64 exec, s[22:23]
	v_cmp_lt_u32_e32 vcc, 3, v9
	s_cbranch_vccz .Lp2_c2_p2done
	s_and_saveexec_b64 s[22:23], vcc
	v_cmp_gt_u32_e32 vcc, 32, v79
	s_andn2_b64 s[36:37], exec, vcc
	s_or_b64 s[38:39], s[38:39], s[36:37]
	s_and_b64 exec, exec, vcc
	v_lshrrev_b32_e32 v13, 16, v39
	v_lshl_add_u32 v13, v13, 5, v79
	v_lshlrev_b32_e32 v13, 2, v13
	v_and_b32_e32 v14, 0xffff, v39
	global_store_dword v13, v14, s[6:7] sc1
	s_mov_b64 exec, s[22:23]
	v_cmp_lt_u32_e32 vcc, 4, v9
	s_cbranch_vccz .Lp2_c2_p2done
	s_and_saveexec_b64 s[22:23], vcc
	v_cmp_gt_u32_e32 vcc, 32, v80
	s_andn2_b64 s[36:37], exec, vcc
	s_or_b64 s[38:39], s[38:39], s[36:37]
	s_and_b64 exec, exec, vcc
	v_lshrrev_b32_e32 v13, 16, v40
	v_lshl_add_u32 v13, v13, 5, v80
	v_lshlrev_b32_e32 v13, 2, v13
	v_and_b32_e32 v14, 0xffff, v40
	global_store_dword v13, v14, s[6:7] sc1
	s_mov_b64 exec, s[22:23]
	v_cmp_lt_u32_e32 vcc, 5, v9
	s_cbranch_vccz .Lp2_c2_p2done
	s_and_saveexec_b64 s[22:23], vcc
	v_cmp_gt_u32_e32 vcc, 32, v81
	s_andn2_b64 s[36:37], exec, vcc
	s_or_b64 s[38:39], s[38:39], s[36:37]
	s_and_b64 exec, exec, vcc
	v_lshrrev_b32_e32 v13, 16, v41
	v_lshl_add_u32 v13, v13, 5, v81
	v_lshlrev_b32_e32 v13, 2, v13
	v_and_b32_e32 v14, 0xffff, v41
	global_store_dword v13, v14, s[6:7] sc1
	s_mov_b64 exec, s[22:23]
	v_cmp_lt_u32_e32 vcc, 6, v9
	s_cbranch_vccz .Lp2_c2_p2done
	s_and_saveexec_b64 s[22:23], vcc
	v_cmp_gt_u32_e32 vcc, 32, v82
	s_andn2_b64 s[36:37], exec, vcc
	s_or_b64 s[38:39], s[38:39], s[36:37]
	s_and_b64 exec, exec, vcc
	v_lshrrev_b32_e32 v13, 16, v42
	v_lshl_add_u32 v13, v13, 5, v82
	v_lshlrev_b32_e32 v13, 2, v13
	v_and_b32_e32 v14, 0xffff, v42
	global_store_dword v13, v14, s[6:7] sc1
	s_mov_b64 exec, s[22:23]
	v_cmp_lt_u32_e32 vcc, 7, v9
	s_cbranch_vccz .Lp2_c2_p2done
	s_and_saveexec_b64 s[22:23], vcc
	v_cmp_gt_u32_e32 vcc, 32, v83
	s_andn2_b64 s[36:37], exec, vcc
	s_or_b64 s[38:39], s[38:39], s[36:37]
	s_and_b64 exec, exec, vcc
	v_lshrrev_b32_e32 v13, 16, v43
	v_lshl_add_u32 v13, v13, 5, v83
	v_lshlrev_b32_e32 v13, 2, v13
	v_and_b32_e32 v14, 0xffff, v43
	global_store_dword v13, v14, s[6:7] sc1
	s_mov_b64 exec, s[22:23]
.Lp2_c2_p2done:
	v_cmp_lt_u32_e32 vcc, 0, v10
	s_cbranch_vccz .Lp2_c3_p2done
	s_and_saveexec_b64 s[22:23], vcc
	v_cmp_gt_u32_e32 vcc, 32, v84
	s_andn2_b64 s[36:37], exec, vcc
	s_or_b64 s[38:39], s[38:39], s[36:37]
	s_and_b64 exec, exec, vcc
	v_lshrrev_b32_e32 v13, 16, v44
	v_lshl_add_u32 v13, v13, 5, v84
	v_lshlrev_b32_e32 v13, 2, v13
	v_and_b32_e32 v14, 0xffff, v44
	global_store_dword v13, v14, s[6:7] sc1
	s_mov_b64 exec, s[22:23]
	v_cmp_lt_u32_e32 vcc, 1, v10
	s_cbranch_vccz .Lp2_c3_p2done
	s_and_saveexec_b64 s[22:23], vcc
	v_cmp_gt_u32_e32 vcc, 32, v85
	s_andn2_b64 s[36:37], exec, vcc
	s_or_b64 s[38:39], s[38:39], s[36:37]
	s_and_b64 exec, exec, vcc
	v_lshrrev_b32_e32 v13, 16, v45
	v_lshl_add_u32 v13, v13, 5, v85
	v_lshlrev_b32_e32 v13, 2, v13
	v_and_b32_e32 v14, 0xffff, v45
	global_store_dword v13, v14, s[6:7] sc1
	s_mov_b64 exec, s[22:23]
	v_cmp_lt_u32_e32 vcc, 2, v10
	s_cbranch_vccz .Lp2_c3_p2done
	s_and_saveexec_b64 s[22:23], vcc
	v_cmp_gt_u32_e32 vcc, 32, v86
	s_andn2_b64 s[36:37], exec, vcc
	s_or_b64 s[38:39], s[38:39], s[36:37]
	s_and_b64 exec, exec, vcc
	v_lshrrev_b32_e32 v13, 16, v46
	v_lshl_add_u32 v13, v13, 5, v86
	v_lshlrev_b32_e32 v13, 2, v13
	v_and_b32_e32 v14, 0xffff, v46
	global_store_dword v13, v14, s[6:7] sc1
	s_mov_b64 exec, s[22:23]
	v_cmp_lt_u32_e32 vcc, 3, v10
	s_cbranch_vccz .Lp2_c3_p2done
	s_and_saveexec_b64 s[22:23], vcc
	v_cmp_gt_u32_e32 vcc, 32, v87
	s_andn2_b64 s[36:37], exec, vcc
	s_or_b64 s[38:39], s[38:39], s[36:37]
	s_and_b64 exec, exec, vcc
	v_lshrrev_b32_e32 v13, 16, v47
	v_lshl_add_u32 v13, v13, 5, v87
	v_lshlrev_b32_e32 v13, 2, v13
	v_and_b32_e32 v14, 0xffff, v47
	global_store_dword v13, v14, s[6:7] sc1
	s_mov_b64 exec, s[22:23]
	v_cmp_lt_u32_e32 vcc, 4, v10
	s_cbranch_vccz .Lp2_c3_p2done
	s_and_saveexec_b64 s[22:23], vcc
	v_cmp_gt_u32_e32 vcc, 32, v88
	s_andn2_b64 s[36:37], exec, vcc
	s_or_b64 s[38:39], s[38:39], s[36:37]
	s_and_b64 exec, exec, vcc
	v_lshrrev_b32_e32 v13, 16, v48
	v_lshl_add_u32 v13, v13, 5, v88
	v_lshlrev_b32_e32 v13, 2, v13
	v_and_b32_e32 v14, 0xffff, v48
	global_store_dword v13, v14, s[6:7] sc1
	s_mov_b64 exec, s[22:23]
	v_cmp_lt_u32_e32 vcc, 5, v10
	s_cbranch_vccz .Lp2_c3_p2done
	s_and_saveexec_b64 s[22:23], vcc
	v_cmp_gt_u32_e32 vcc, 32, v89
	s_andn2_b64 s[36:37], exec, vcc
	s_or_b64 s[38:39], s[38:39], s[36:37]
	s_and_b64 exec, exec, vcc
	v_lshrrev_b32_e32 v13, 16, v49
	v_lshl_add_u32 v13, v13, 5, v89
	v_lshlrev_b32_e32 v13, 2, v13
	v_and_b32_e32 v14, 0xffff, v49
	global_store_dword v13, v14, s[6:7] sc1
	s_mov_b64 exec, s[22:23]
	v_cmp_lt_u32_e32 vcc, 6, v10
	s_cbranch_vccz .Lp2_c3_p2done
	s_and_saveexec_b64 s[22:23], vcc
	v_cmp_gt_u32_e32 vcc, 32, v90
	s_andn2_b64 s[36:37], exec, vcc
	s_or_b64 s[38:39], s[38:39], s[36:37]
	s_and_b64 exec, exec, vcc
	v_lshrrev_b32_e32 v13, 16, v50
	v_lshl_add_u32 v13, v13, 5, v90
	v_lshlrev_b32_e32 v13, 2, v13
	v_and_b32_e32 v14, 0xffff, v50
	global_store_dword v13, v14, s[6:7] sc1
	s_mov_b64 exec, s[22:23]
	v_cmp_lt_u32_e32 vcc, 7, v10
	s_cbranch_vccz .Lp2_c3_p2done
	s_and_saveexec_b64 s[22:23], vcc
	v_cmp_gt_u32_e32 vcc, 32, v91
	s_andn2_b64 s[36:37], exec, vcc
	s_or_b64 s[38:39], s[38:39], s[36:37]
	s_and_b64 exec, exec, vcc
	v_lshrrev_b32_e32 v13, 16, v51
	v_lshl_add_u32 v13, v13, 5, v91
	v_lshlrev_b32_e32 v13, 2, v13
	v_and_b32_e32 v14, 0xffff, v51
	global_store_dword v13, v14, s[6:7] sc1
	s_mov_b64 exec, s[22:23]

.Lp2_c4_p1done:
	s_waitcnt lgkmcnt(0)
	v_cmp_lt_u32_e32 vcc, 0, v11
	s_cbranch_vccz .Lp2_c4_p2done
	s_and_saveexec_b64 s[22:23], vcc
	v_cmp_gt_u32_e32 vcc, 32, v60
	s_andn2_b64 s[36:37], exec, vcc
	s_or_b64 s[38:39], s[38:39], s[36:37]
	s_and_b64 exec, exec, vcc
	v_lshrrev_b32_e32 v13, 16, v52
	v_lshl_add_u32 v13, v13, 5, v60
	v_lshlrev_b32_e32 v13, 2, v13
	v_and_b32_e32 v14, 0xffff, v52
	global_store_dword v13, v14, s[6:7] sc1
	s_mov_b64 exec, s[22:23]
	v_cmp_lt_u32_e32 vcc, 1, v11
	s_cbranch_vccz .Lp2_c4_p2done
	s_and_saveexec_b64 s[22:23], vcc
	v_cmp_gt_u32_e32 vcc, 32, v61
	s_andn2_b64 s[36:37], exec, vcc
	s_or_b64 s[38:39], s[38:39], s[36:37]
	s_and_b64 exec, exec, vcc
	v_lshrrev_b32_e32 v13, 16, v53
	v_lshl_add_u32 v13, v13, 5, v61
	v_lshlrev_b32_e32 v13, 2, v13
	v_and_b32_e32 v14, 0xffff, v53
	global_store_dword v13, v14, s[6:7] sc1
	s_mov_b64 exec, s[22:23]
	v_cmp_lt_u32_e32 vcc, 2, v11
	s_cbranch_vccz .Lp2_c4_p2done
	s_and_saveexec_b64 s[22:23], vcc
	v_cmp_gt_u32_e32 vcc, 32, v62
	s_andn2_b64 s[36:37], exec, vcc
	s_or_b64 s[38:39], s[38:39], s[36:37]
	s_and_b64 exec, exec, vcc
	v_lshrrev_b32_e32 v13, 16, v54
	v_lshl_add_u32 v13, v13, 5, v62
	v_lshlrev_b32_e32 v13, 2, v13
	v_and_b32_e32 v14, 0xffff, v54
	global_store_dword v13, v14, s[6:7] sc1
	s_mov_b64 exec, s[22:23]
	v_cmp_lt_u32_e32 vcc, 3, v11
	s_cbranch_vccz .Lp2_c4_p2done
	s_and_saveexec_b64 s[22:23], vcc
	v_cmp_gt_u32_e32 vcc, 32, v63
	s_andn2_b64 s[36:37], exec, vcc
	s_or_b64 s[38:39], s[38:39], s[36:37]
	s_and_b64 exec, exec, vcc
	v_lshrrev_b32_e32 v13, 16, v55
	v_lshl_add_u32 v13, v13, 5, v63
	v_lshlrev_b32_e32 v13, 2, v13
	v_and_b32_e32 v14, 0xffff, v55
	global_store_dword v13, v14, s[6:7] sc1
	s_mov_b64 exec, s[22:23]
	v_cmp_lt_u32_e32 vcc, 4, v11
	s_cbranch_vccz .Lp2_c4_p2done
	s_and_saveexec_b64 s[22:23], vcc
	v_cmp_gt_u32_e32 vcc, 32, v64
	s_andn2_b64 s[36:37], exec, vcc
	s_or_b64 s[38:39], s[38:39], s[36:37]
	s_and_b64 exec, exec, vcc
	v_lshrrev_b32_e32 v13, 16, v56
	v_lshl_add_u32 v13, v13, 5, v64
	v_lshlrev_b32_e32 v13, 2, v13
	v_and_b32_e32 v14, 0xffff, v56
	global_store_dword v13, v14, s[6:7] sc1
	s_mov_b64 exec, s[22:23]
	v_cmp_lt_u32_e32 vcc, 5, v11
	s_cbranch_vccz .Lp2_c4_p2done
	s_and_saveexec_b64 s[22:23], vcc
	v_cmp_gt_u32_e32 vcc, 32, v65
	s_andn2_b64 s[36:37], exec, vcc
	s_or_b64 s[38:39], s[38:39], s[36:37]
	s_and_b64 exec, exec, vcc
	v_lshrrev_b32_e32 v13, 16, v57
	v_lshl_add_u32 v13, v13, 5, v65
	v_lshlrev_b32_e32 v13, 2, v13
	v_and_b32_e32 v14, 0xffff, v57
	global_store_dword v13, v14, s[6:7] sc1
	s_mov_b64 exec, s[22:23]
	v_cmp_lt_u32_e32 vcc, 6, v11
	s_cbranch_vccz .Lp2_c4_p2done
	s_and_saveexec_b64 s[22:23], vcc
	v_cmp_gt_u32_e32 vcc, 32, v66
	s_andn2_b64 s[36:37], exec, vcc
	s_or_b64 s[38:39], s[38:39], s[36:37]
	s_and_b64 exec, exec, vcc
	v_lshrrev_b32_e32 v13, 16, v58
	v_lshl_add_u32 v13, v13, 5, v66
	v_lshlrev_b32_e32 v13, 2, v13
	v_and_b32_e32 v14, 0xffff, v58
	global_store_dword v13, v14, s[6:7] sc1
	s_mov_b64 exec, s[22:23]
	v_cmp_lt_u32_e32 vcc, 7, v11
	s_cbranch_vccz .Lp2_c4_p2done
	s_and_saveexec_b64 s[22:23], vcc
	v_cmp_gt_u32_e32 vcc, 32, v67
	s_andn2_b64 s[36:37], exec, vcc
	s_or_b64 s[38:39], s[38:39], s[36:37]
	s_and_b64 exec, exec, vcc
	v_lshrrev_b32_e32 v13, 16, v59
	v_lshl_add_u32 v13, v13, 5, v67
	v_lshlrev_b32_e32 v13, 2, v13
	v_and_b32_e32 v14, 0xffff, v59
	global_store_dword v13, v14, s[6:7] sc1
	s_mov_b64 exec, s[22:23]

.Lp2_c0_tail:
	v_cmp_lt_u32_e32 vcc, v15, v7
	s_and_saveexec_b64 s[22:23], vcc
	s_cbranch_execz .Lp2_c0_tailend
	v_lshl_add_u32 v13, v15, 2, v2
	global_load_dword v16, v13, s[26:27] sc1
	s_waitcnt vmcnt(0)
	v_bfe_u32 v13, v16, 16, 7
	v_lshlrev_b32_e32 v13, 2, v13
	ds_add_rtn_u32 v17, v13, v12
	s_waitcnt lgkmcnt(0)
	v_cmp_gt_u32_e32 vcc, 32, v17
	s_andn2_b64 s[36:37], exec, vcc
	s_or_b64 s[38:39], s[38:39], s[36:37]
	s_and_b64 exec, exec, vcc
	v_lshrrev_b32_e32 v13, 16, v16
	v_lshl_add_u32 v13, v13, 5, v17
	v_lshlrev_b32_e32 v13, 2, v13
	v_and_b32_e32 v14, 0xffff, v16
	global_store_dword v13, v14, s[6:7] sc1
	s_mov_b64 exec, s[22:23]
	v_add_u32_e32 v15, 1, v15
	s_branch .Lp2_c0_tail

.Lp2_c1_tail:
	v_cmp_lt_u32_e32 vcc, v15, v8
	s_and_saveexec_b64 s[22:23], vcc
	s_cbranch_execz .Lp2_c1_tailend
	v_lshl_add_u32 v13, v15, 2, v3
	global_load_dword v16, v13, s[26:27] sc1
	s_waitcnt vmcnt(0)
	v_bfe_u32 v13, v16, 16, 7
	v_lshlrev_b32_e32 v13, 2, v13
	ds_add_rtn_u32 v17, v13, v12
	s_waitcnt lgkmcnt(0)
	v_cmp_gt_u32_e32 vcc, 32, v17
	s_andn2_b64 s[36:37], exec, vcc
	s_or_b64 s[38:39], s[38:39], s[36:37]
	s_and_b64 exec, exec, vcc
	v_lshrrev_b32_e32 v13, 16, v16
	v_lshl_add_u32 v13, v13, 5, v17
	v_lshlrev_b32_e32 v13, 2, v13
	v_and_b32_e32 v14, 0xffff, v16
	global_store_dword v13, v14, s[6:7] sc1
	s_mov_b64 exec, s[22:23]
	v_add_u32_e32 v15, 1, v15
	s_branch .Lp2_c1_tail

.Lp2_c2_tail:
	v_cmp_lt_u32_e32 vcc, v15, v9
	s_and_saveexec_b64 s[22:23], vcc
	s_cbranch_execz .Lp2_c2_tailend
	v_lshl_add_u32 v13, v15, 2, v4
	global_load_dword v16, v13, s[26:27] sc1
	s_waitcnt vmcnt(0)
	v_bfe_u32 v13, v16, 16, 7
	v_lshlrev_b32_e32 v13, 2, v13
	ds_add_rtn_u32 v17, v13, v12
	s_waitcnt lgkmcnt(0)
	v_cmp_gt_u32_e32 vcc, 32, v17
	s_andn2_b64 s[36:37], exec, vcc
	s_or_b64 s[38:39], s[38:39], s[36:37]
	s_and_b64 exec, exec, vcc
	v_lshrrev_b32_e32 v13, 16, v16
	v_lshl_add_u32 v13, v13, 5, v17
	v_lshlrev_b32_e32 v13, 2, v13
	v_and_b32_e32 v14, 0xffff, v16
	global_store_dword v13, v14, s[6:7] sc1
	s_mov_b64 exec, s[22:23]
	v_add_u32_e32 v15, 1, v15
	s_branch .Lp2_c2_tail

.Lp2_c3_tail:
	v_cmp_lt_u32_e32 vcc, v15, v10
	s_and_saveexec_b64 s[22:23], vcc
	s_cbranch_execz .Lp2_c3_tailend
	v_lshl_add_u32 v13, v15, 2, v5
	global_load_dword v16, v13, s[26:27] sc1
	s_waitcnt vmcnt(0)
	v_bfe_u32 v13, v16, 16, 7
	v_lshlrev_b32_e32 v13, 2, v13
	ds_add_rtn_u32 v17, v13, v12
	s_waitcnt lgkmcnt(0)
	v_cmp_gt_u32_e32 vcc, 32, v17
	s_andn2_b64 s[36:37], exec, vcc
	s_or_b64 s[38:39], s[38:39], s[36:37]
	s_and_b64 exec, exec, vcc
	v_lshrrev_b32_e32 v13, 16, v16
	v_lshl_add_u32 v13, v13, 5, v17
	v_lshlrev_b32_e32 v13, 2, v13
	v_and_b32_e32 v14, 0xffff, v16
	global_store_dword v13, v14, s[6:7] sc1
	s_mov_b64 exec, s[22:23]
	v_add_u32_e32 v15, 1, v15
	s_branch .Lp2_c3_tail

.Lp2_c4_tail:
	v_cmp_lt_u32_e32 vcc, v15, v11
	s_and_saveexec_b64 s[22:23], vcc
	s_cbranch_execz .Lp2_c4_tailend
	v_lshl_add_u32 v13, v15, 2, v6
	global_load_dword v16, v13, s[26:27] sc1
	s_waitcnt vmcnt(0)
	v_bfe_u32 v13, v16, 16, 7
	v_lshlrev_b32_e32 v13, 2, v13
	ds_add_rtn_u32 v17, v13, v12
	s_waitcnt lgkmcnt(0)
	v_cmp_gt_u32_e32 vcc, 32, v17
	s_andn2_b64 s[36:37], exec, vcc
	s_or_b64 s[38:39], s[38:39], s[36:37]
	s_and_b64 exec, exec, vcc
	v_lshrrev_b32_e32 v13, 16, v16
	v_lshl_add_u32 v13, v13, 5, v17
	v_lshlrev_b32_e32 v13, 2, v13
	v_and_b32_e32 v14, 0xffff, v16
	global_store_dword v13, v14, s[6:7] sc1
	s_mov_b64 exec, s[22:23]
	v_add_u32_e32 v15, 1, v15
	s_branch .Lp2_c4_tail
